# P7/P8 epilogue bias prefetched into spare LDS by one wave (LDS-DMA) at unit start; epilogue reads it with ds_read_b128 instead of global loads behind vmcnt(0)
# baseline (speedup 1.0000x reference)
;     __device__ __forceinline__ const char* a_base(const Unit& u) const { return GATHER ? A : A + ((size_t)__builtin_amdgcn_readfirstlane(poff[u.e]) + (size_t)u.pm * BM) * ROWB; }
;     __device__ __forceinline__ void operator()(const f32x4 (&acc)[2][2][4][2], const Unit& u, int wr, int wc, int fr, int fq) const {
;         const int row0 = poff[u.e] + u.pm * BM + wr * 64 + fr, col0 = u.pn * BM + wc * 32 + 8 * fq;
;         const float* bp = bias + (size_t)u.e * (2 * DFF) + col0;
; template <class Epi, class Sched>
; __device__ __forceinline__ void gemm_phase(LAS unsigned char* lds, const Sched& S, const Epi& E) {
;     ...
;     for (;;) {
;         const bool has_next = S.next(ui + 1, nxt);
;         const char* nA = has_next ? S.a_base(nxt) : cA; const char* nB = has_next ? S.b_base(nxt) : cB;
;         if (has_next) S.idx_prefetch(nxt, ldsb + IDX_OFF, wid, lane);
.LBB0_1002:
	v_readlane_b32 s98, v253, 0
	s_lshr_b32 s98, s98, 6
	s_cmp_lg_u32 s98, 7
	s_cbranch_scc1 .Lbp7_skip
	s_lshl_b32 s98, s52, 14
	s_lshl_b32 s99, s54, 10
	s_add_i32 s98, s98, s99
	s_add_u32 s98, s48, s98
	s_addc_u32 s99, s49, 0
	s_and_b32 s100, s25, 1
	s_lshl_b32 s100, s100, 10
	s_add_i32 s100, s100, 0x22800
	v_mbcnt_lo_u32_b32 v255, -1, 0
	v_mbcnt_hi_u32_b32 v255, -1, v255
	v_lshlrev_b32_e32 v255, 4, v255
	s_mov_b32 s101, m0
	s_mov_b32 m0, s100
	s_nop 0
	global_load_lds_dwordx4 v255, s[98:99]
	s_mov_b32 m0, s101

; __device__ __forceinline__ unsigned pk4_fp8(float a, float b, float c, float d) { int p = 0; p = __builtin_amdgcn_cvt_pk_fp8_f32(a, b, p, false); p = __builtin_amdgcn_cvt_pk_fp8_f32(c, d, p, true); return (unsigned)p; }
;     __device__ __forceinline__ float act1(float g, float up1) const { g = fminf(g, 7.f); up1 = fminf(fmaxf(up1, -6.f), 8.f); return g * __builtin_amdgcn_rcpf(1.f + __builtin_amdgcn_exp2f(g * (-1.702f * 1.44269504f))) * up1; }
;     __device__ __forceinline__ void operator()(const f32x4 (&acc)[2][2][4][2], const Unit& u, int wr, int wc, int fr, int fq) const {
;         const int row0 = poff[u.e] + u.pm * BM + wr * 64 + fr, col0 = u.pn * BM + wc * 32 + 8 * fq;
;         const float* bp = bias + (size_t)u.e * (2 * DFF) + col0;
;         f32x4 bv[2][2];
; #pragma unroll
;         for (int bj = 0; bj < 2; ++bj)
; #pragma unroll
;             for (int n = 0; n < 2; ++n) { bv[bj][n] = *(const f32x4*)(bp + bj * HALF + 4 * n); bv[bj][n].y += 1.f; bv[bj][n].w += 1.f; }
; #pragma unroll
;         for (int ai = 0; ai < 2; ++ai)
; #pragma unroll
;             for (int m = 0; m < 4; ++m) { unsigned char* rowp = ACT + (size_t)(row0 + ai * HALF + m * 16) * DFF + (col0 >> 1);
; #pragma unroll
;                 for (int bj = 0; bj < 2; ++bj) { const f32x4 v0 = acc[ai][bj][m][0] * WINV + bv[bj][0], v1 = acc[ai][bj][m][1] * WINV + bv[bj][1];
;                     *(unsigned*)(rowp + bj * (HALF / 2)) = pk4_fp8(act1(v0[0], v0[1]), act1(v0[2], v0[3]), act1(v1[0], v1[1]), act1(v1[2], v1[3])); } }
.LBB0_1013:
	s_lshl_b32 s12, s52, 2
	s_add_i32 s12, s12, 0
	s_add_i32 s12, s12, 0x20300
	v_mov_b32_e32 v28, v1
	v_mov_b32_e32 v2, s12
	ds_read_b32 v29, v2
	s_lshl_b32 s12, s54, 8
	v_ashrrev_i32_e32 v2, 1, v28
	s_ashr_i32 s53, s52, 31
	v_and_b32_e32 v2, -8, v2
	s_or_b32 s12, s12, s22
	s_lshl_b32 s41, s79, 8
	v_add_u32_e32 v18, s12, v2
	s_lshl_b64 s[12:13], s[52:53], 14
	s_add_u32 s12, s48, s12
	s_addc_u32 s13, s49, s13
	v_ashrrev_i32_e32 v19, 31, v18
	s_and_b32 s100, s25, 1
	s_xor_b32 s100, s100, 1
	s_lshl_b32 s100, s100, 10
	s_add_i32 s100, s100, 0x22800
	v_and_b32_e32 v6, 0xff, v18
	v_lshlrev_b32_e32 v6, 2, v6
	v_add_u32_e32 v6, s100, v6
	ds_read_b128 v[10:13], v6 offset:16
	ds_read_b128 v[14:17], v6
	ds_read_b128 v[2:5], v6 offset:528
	ds_read_b128 v[6:9], v6 offset:512
	s_and_b64 vcc, exec, s[4:5]
	s_cbranch_vccz .LBB0_1015
	s_barrier
.LBB0_1015:
	s_add_i32 s41, s41, s94
	v_ashrrev_i32_e32 v18, 1, v18
	v_ashrrev_i32_e32 v19, 31, v18
	v_lshl_add_u64 v[18:19], s[20:21], 0, v[18:19]
	s_mov_b64 s[12:13], 0x8000
	s_mov_b64 s[52:53], -1
	s_waitcnt lgkmcnt(0)
	v_mov_b32_e32 v20, v15
	v_mov_b32_e32 v21, v17
	v_pk_add_f32 v[24:25], v[20:21], 1.0 op_sel_hi:[1,0]
	v_mov_b32_e32 v20, v11
	v_mov_b32_e32 v21, v13
	v_pk_add_f32 v[26:27], v[20:21], 1.0 op_sel_hi:[1,0]
	v_mov_b32_e32 v15, v24
	v_mov_b32_e32 v17, v25
	v_pk_fma_f32 v[24:25], v[190:191], s[38:39], v[14:15] op_sel_hi:[1,0,1]
	v_mov_b32_e32 v11, v26
	v_mov_b32_e32 v13, v27
	v_pk_fma_f32 v[26:27], v[186:187], s[38:39], v[10:11] op_sel_hi:[1,0,1]
	v_pk_fma_f32 v[30:31], v[188:189], s[38:39], v[12:13] op_sel_hi:[1,0,1]
	v_mov_b32_e32 v20, v7
	v_mov_b32_e32 v21, v9
	v_pk_add_f32 v[22:23], v[20:21], 1.0 op_sel_hi:[1,0]
	v_mov_b32_e32 v20, v3
	v_and_or_b32 v3, v28, 15, s41
	s_waitcnt lgkmcnt(0)
	v_add_u32_e32 v28, v3, v29
	v_min_f32_e32 v3, 0x40e00000, v24
	v_mul_f32_e32 v7, 0xc01d265f, v3
	v_exp_f32_e32 v7, v7
	v_ashrrev_i32_e32 v29, 31, v28
	v_lshlrev_b64 v[28:29], 11, v[28:29]
	v_mov_b32_e32 v21, v5
	v_add_f32_e32 v7, 1.0, v7
	v_rcp_f32_e32 v7, v7
	v_lshl_add_u64 v[18:19], v[18:19], 0, v[28:29]
	v_pk_fma_f32 v[28:29], v[192:193], s[38:39], v[16:17] op_sel_hi:[1,0,1]
	v_med3_f32 v5, v25, s23, v200
	v_mul_f32_e32 v3, v3, v7
	v_mul_f32_e32 v3, v5, v3
	v_min_f32_e32 v5, 0x40e00000, v28
	v_mul_f32_e32 v9, 0xc01d265f, v5
	v_exp_f32_e32 v9, v9
	v_med3_f32 v7, v29, s23, v200
	v_pk_add_f32 v[20:21], v[20:21], 1.0 op_sel_hi:[1,0]
	v_add_f32_e32 v9, 1.0, v9
	v_rcp_f32_e32 v9, v9
	s_nop 0
	v_mul_f32_e32 v5, v5, v9
	v_mul_f32_e32 v5, v7, v5
	v_min_f32_e32 v7, 0x40e00000, v26
	v_mul_f32_e32 v24, 0xc01d265f, v7
	v_exp_f32_e32 v24, v24
	v_med3_f32 v9, v27, s23, v200
	v_add_f32_e32 v24, 1.0, v24
	v_rcp_f32_e32 v24, v24
	s_nop 0
	v_mul_f32_e32 v7, v7, v24
	v_mul_f32_e32 v7, v9, v7
	v_min_f32_e32 v9, 0x40e00000, v30
	v_mul_f32_e32 v25, 0xc01d265f, v9
	v_exp_f32_e32 v25, v25
	v_med3_f32 v24, v31, s23, v200
	v_add_f32_e32 v25, 1.0, v25
	v_rcp_f32_e32 v25, v25
	s_nop 0
	v_mul_f32_e32 v9, v9, v25
	v_mul_f32_e32 v9, v24, v9
	v_mov_b32_e32 v24, v195
	v_cvt_pk_fp8_f32 v24, v3, v5
	v_mov_b32_e32 v3, v20
	v_mov_b32_e32 v5, v21
	v_pk_fma_f32 v[20:21], v[178:179], s[38:39], v[2:3] op_sel_hi:[1,0,1]
	v_cvt_pk_fp8_f32 v24, v7, v9 op_sel:[0,0,1]
	v_mov_b32_e32 v7, v22
	v_pk_fma_f32 v[26:27], v[182:183], s[38:39], v[6:7] op_sel_hi:[1,0,1]
	v_mov_b32_e32 v9, v23
	v_min_f32_e32 v26, 0x40e00000, v26
	v_mul_f32_e32 v28, 0xc01d265f, v26
	v_exp_f32_e32 v28, v28
	global_store_dword v[18:19], v24, off
	v_pk_fma_f32 v[24:25], v[184:185], s[38:39], v[8:9] op_sel_hi:[1,0,1]
	v_med3_f32 v27, v27, s23, v200
	v_add_f32_e32 v28, 1.0, v28
	v_rcp_f32_e32 v28, v28
	v_min_f32_e32 v24, 0x40e00000, v24
	v_med3_f32 v25, v25, s23, v200
	v_min_f32_e32 v20, 0x40e00000, v20
	v_mul_f32_e32 v26, v26, v28
	v_mul_f32_e32 v26, v27, v26
	v_mul_f32_e32 v27, 0xc01d265f, v24
	v_exp_f32_e32 v27, v27
	v_pk_fma_f32 v[22:23], v[180:181], s[38:39], v[4:5] op_sel_hi:[1,0,1]
	v_med3_f32 v21, v21, s23, v200
	v_pk_fma_f32 v[28:29], v[170:171], s[38:39], v[10:11] op_sel_hi:[1,0,1]
	v_add_f32_e32 v27, 1.0, v27
	v_rcp_f32_e32 v27, v27
	s_nop 0
	v_mul_f32_e32 v24, v24, v27
	v_mul_f32_e32 v24, v25, v24
	v_mul_f32_e32 v25, 0xc01d265f, v20
	v_exp_f32_e32 v25, v25
	s_nop 0
	v_add_f32_e32 v25, 1.0, v25
	v_rcp_f32_e32 v25, v25
	s_nop 0
	v_mul_f32_e32 v20, v20, v25
	v_mul_f32_e32 v20, v21, v20
	v_min_f32_e32 v21, 0x40e00000, v22
	v_med3_f32 v22, v23, s23, v200
	v_mul_f32_e32 v23, 0xc01d265f, v21
	v_exp_f32_e32 v23, v23
	s_nop 0
	v_add_f32_e32 v23, 1.0, v23
	v_rcp_f32_e32 v23, v23
	s_nop 0
	v_mul_f32_e32 v21, v21, v23
	v_mul_f32_e32 v21, v22, v21
	v_mov_b32_e32 v22, v195
	v_cvt_pk_fp8_f32 v22, v26, v24
	v_pk_fma_f32 v[24:25], v[174:175], s[38:39], v[14:15] op_sel_hi:[1,0,1]
	v_pk_fma_f32 v[26:27], v[172:173], s[38:39], v[12:13] op_sel_hi:[1,0,1]
	v_min_f32_e32 v24, 0x40e00000, v24
	v_mul_f32_e32 v30, 0xc01d265f, v24
	v_exp_f32_e32 v30, v30
	v_cvt_pk_fp8_f32 v22, v20, v21 op_sel:[0,0,1]
	v_med3_f32 v25, v25, s23, v200
	v_lshl_add_u64 v[20:21], v[18:19], 0, s[12:13]
	v_add_f32_e32 v30, 1.0, v30
	v_rcp_f32_e32 v30, v30
	global_store_dword v[18:19], v22, off offset:64
	v_pk_fma_f32 v[22:23], v[176:177], s[38:39], v[16:17] op_sel_hi:[1,0,1]
	s_mov_b32 s12, 0x8000
	v_mul_f32_e32 v24, v24, v30
	v_min_f32_e32 v22, 0x40e00000, v22
	v_mul_f32_e32 v24, v25, v24
	v_mul_f32_e32 v25, 0xc01d265f, v22
	v_exp_f32_e32 v25, v25
	v_med3_f32 v23, v23, s23, v200
	v_add_f32_e32 v25, 1.0, v25
	v_rcp_f32_e32 v25, v25
	s_nop 0
	v_mul_f32_e32 v22, v22, v25
	v_mul_f32_e32 v22, v23, v22
	v_min_f32_e32 v23, 0x40e00000, v28
	v_mul_f32_e32 v28, 0xc01d265f, v23
	v_exp_f32_e32 v28, v28
	v_med3_f32 v25, v29, s23, v200
; __device__ __forceinline__ unsigned pk4_fp8(float a, float b, float c, float d) { int p = 0; p = __builtin_amdgcn_cvt_pk_fp8_f32(a, b, p, false); p = __builtin_amdgcn_cvt_pk_fp8_f32(c, d, p, true); return (unsigned)p; }
;     __device__ __forceinline__ float act1(float g, float up1) const { g = fminf(g, 7.f); up1 = fminf(fmaxf(up1, -6.f), 8.f); return g * __builtin_amdgcn_rcpf(1.f + __builtin_amdgcn_exp2f(g * (-1.702f * 1.44269504f))) * up1; }
;     __device__ __forceinline__ void operator()(const f32x4 (&acc)[2][2][4][2], const Unit& u, int wr, int wc, int fr, int fq) const {
;     ...
;         for (int ai = 0; ai < 2; ++ai)
; #pragma unroll
;             for (int m = 0; m < 4; ++m) { unsigned char* rowp = ACT + (size_t)(row0 + ai * HALF + m * 16) * DFF + (col0 >> 1);
; #pragma unroll
;                 for (int bj = 0; bj < 2; ++bj) { const f32x4 v0 = acc[ai][bj][m][0] * WINV + bv[bj][0], v1 = acc[ai][bj][m][1] * WINV + bv[bj][1];
;                     *(unsigned*)(rowp + bj * (HALF / 2)) = pk4_fp8(act1(v0[0], v0[1]), act1(v0[2], v0[3]), act1(v1[0], v1[1]), act1(v1[2], v1[3])); } }
	v_add_f32_e32 v28, 1.0, v28
	v_rcp_f32_e32 v28, v28
	s_nop 0
	v_mul_f32_e32 v23, v23, v28
	v_mul_f32_e32 v23, v25, v23
	v_min_f32_e32 v25, 0x40e00000, v26
	v_med3_f32 v26, v27, s23, v200
	v_mul_f32_e32 v27, 0xc01d265f, v25
	v_exp_f32_e32 v27, v27
	v_pk_fma_f32 v[28:29], v[162:163], s[38:39], v[2:3] op_sel_hi:[1,0,1]
	v_add_f32_e32 v27, 1.0, v27
	v_rcp_f32_e32 v27, v27
	s_nop 0
	v_mul_f32_e32 v25, v25, v27
	v_mul_f32_e32 v25, v26, v25
	v_mov_b32_e32 v26, v195
	v_cvt_pk_fp8_f32 v26, v24, v22
	v_add_co_u32_e32 v22, vcc, s12, v18
	s_mov_b64 s[12:13], 0x10000
	v_cvt_pk_fp8_f32 v26, v23, v25 op_sel:[0,0,1]
	v_pk_fma_f32 v[24:25], v[166:167], s[38:39], v[6:7] op_sel_hi:[1,0,1]
	v_addc_co_u32_e32 v23, vcc, 0, v19, vcc
	v_min_f32_e32 v24, 0x40e00000, v24
	v_mul_f32_e32 v30, 0xc01d265f, v24
	v_exp_f32_e32 v30, v30
	global_store_dword v[22:23], v26, off
	v_pk_fma_f32 v[22:23], v[168:169], s[38:39], v[8:9] op_sel_hi:[1,0,1]
	v_med3_f32 v25, v25, s23, v200
	v_add_f32_e32 v30, 1.0, v30
	v_rcp_f32_e32 v30, v30
	v_min_f32_e32 v22, 0x40e00000, v22
	v_med3_f32 v23, v23, s23, v200
	v_pk_fma_f32 v[26:27], v[164:165], s[38:39], v[4:5] op_sel_hi:[1,0,1]
	v_mul_f32_e32 v24, v24, v30
	v_mul_f32_e32 v24, v25, v24
	v_mul_f32_e32 v25, 0xc01d265f, v22
	v_exp_f32_e32 v25, v25
	s_nop 0
	v_add_f32_e32 v25, 1.0, v25
	v_rcp_f32_e32 v25, v25
	s_nop 0
	v_mul_f32_e32 v22, v22, v25
	v_mul_f32_e32 v22, v23, v22
	v_min_f32_e32 v23, 0x40e00000, v28
	v_mul_f32_e32 v28, 0xc01d265f, v23
	v_exp_f32_e32 v28, v28
	v_med3_f32 v25, v29, s23, v200
	v_add_f32_e32 v28, 1.0, v28
	v_rcp_f32_e32 v28, v28
	s_nop 0
	v_mul_f32_e32 v23, v23, v28
	v_mul_f32_e32 v23, v25, v23
	v_min_f32_e32 v25, 0x40e00000, v26
	v_med3_f32 v26, v27, s23, v200
	v_mul_f32_e32 v27, 0xc01d265f, v25
	v_exp_f32_e32 v27, v27
	v_pk_fma_f32 v[28:29], v[154:155], s[38:39], v[10:11] op_sel_hi:[1,0,1]
	v_add_f32_e32 v27, 1.0, v27
	v_rcp_f32_e32 v27, v27
	s_nop 0
	v_mul_f32_e32 v25, v25, v27
	v_mul_f32_e32 v25, v26, v25
	v_mov_b32_e32 v26, v195
	v_cvt_pk_fp8_f32 v26, v24, v22
	v_cvt_pk_fp8_f32 v26, v23, v25 op_sel:[0,0,1]
	v_pk_fma_f32 v[24:25], v[158:159], s[38:39], v[14:15] op_sel_hi:[1,0,1]
	v_pk_fma_f32 v[22:23], v[160:161], s[38:39], v[16:17] op_sel_hi:[1,0,1]
	v_min_f32_e32 v24, 0x40e00000, v24
	v_mul_f32_e32 v30, 0xc01d265f, v24
	v_exp_f32_e32 v30, v30
	v_med3_f32 v25, v25, s23, v200
	v_min_f32_e32 v22, 0x40e00000, v22
	v_med3_f32 v23, v23, s23, v200
	v_add_f32_e32 v30, 1.0, v30
	v_rcp_f32_e32 v30, v30
	global_store_dword v[20:21], v26, off offset:64
	v_pk_fma_f32 v[26:27], v[156:157], s[38:39], v[12:13] op_sel_hi:[1,0,1]
	v_lshl_add_u64 v[20:21], v[18:19], 0, s[12:13]
	v_mul_f32_e32 v24, v24, v30
	v_mul_f32_e32 v24, v25, v24
	v_mul_f32_e32 v25, 0xc01d265f, v22
	v_exp_f32_e32 v25, v25
	s_mov_b32 s12, 0x10000
	v_add_f32_e32 v25, 1.0, v25
	v_rcp_f32_e32 v25, v25
	s_nop 0
	v_mul_f32_e32 v22, v22, v25
	v_mul_f32_e32 v22, v23, v22
	v_min_f32_e32 v23, 0x40e00000, v28
	v_mul_f32_e32 v28, 0xc01d265f, v23
	v_exp_f32_e32 v28, v28
	v_med3_f32 v25, v29, s23, v200
	v_add_f32_e32 v28, 1.0, v28
	v_rcp_f32_e32 v28, v28
	s_nop 0
	v_mul_f32_e32 v23, v23, v28
	v_mul_f32_e32 v23, v25, v23
	v_min_f32_e32 v25, 0x40e00000, v26
	v_med3_f32 v26, v27, s23, v200
	v_mul_f32_e32 v27, 0xc01d265f, v25
	v_exp_f32_e32 v27, v27
	v_pk_fma_f32 v[28:29], v[146:147], s[38:39], v[2:3] op_sel_hi:[1,0,1]
	v_add_f32_e32 v27, 1.0, v27
	v_rcp_f32_e32 v27, v27
	s_nop 0
	v_mul_f32_e32 v25, v25, v27
	v_mul_f32_e32 v25, v26, v25
	v_mov_b32_e32 v26, v195
	v_cvt_pk_fp8_f32 v26, v24, v22
	v_add_co_u32_e32 v22, vcc, s12, v18
	s_mov_b64 s[12:13], 0x18000
	v_cvt_pk_fp8_f32 v26, v23, v25 op_sel:[0,0,1]
	v_pk_fma_f32 v[24:25], v[150:151], s[38:39], v[6:7] op_sel_hi:[1,0,1]
	v_addc_co_u32_e32 v23, vcc, 0, v19, vcc
	v_min_f32_e32 v24, 0x40e00000, v24
	v_mul_f32_e32 v30, 0xc01d265f, v24
	v_exp_f32_e32 v30, v30
	global_store_dword v[22:23], v26, off
	v_pk_fma_f32 v[22:23], v[152:153], s[38:39], v[8:9] op_sel_hi:[1,0,1]
	v_med3_f32 v25, v25, s23, v200
	v_add_f32_e32 v30, 1.0, v30
	v_rcp_f32_e32 v30, v30
	v_min_f32_e32 v22, 0x40e00000, v22
	v_med3_f32 v23, v23, s23, v200
	v_pk_fma_f32 v[26:27], v[148:149], s[38:39], v[4:5] op_sel_hi:[1,0,1]
	v_mul_f32_e32 v24, v24, v30
	v_mul_f32_e32 v24, v25, v24
	v_mul_f32_e32 v25, 0xc01d265f, v22
	v_exp_f32_e32 v25, v25
	s_nop 0
	v_add_f32_e32 v25, 1.0, v25
	v_rcp_f32_e32 v25, v25
	s_nop 0
	v_mul_f32_e32 v22, v22, v25
	v_mul_f32_e32 v22, v23, v22
	v_min_f32_e32 v23, 0x40e00000, v28
	v_mul_f32_e32 v28, 0xc01d265f, v23
	v_exp_f32_e32 v28, v28
	v_med3_f32 v25, v29, s23, v200
	v_add_f32_e32 v28, 1.0, v28
	v_rcp_f32_e32 v28, v28
	s_nop 0
	v_mul_f32_e32 v23, v23, v28
	v_mul_f32_e32 v23, v25, v23
	v_min_f32_e32 v25, 0x40e00000, v26
	v_med3_f32 v26, v27, s23, v200
	v_mul_f32_e32 v27, 0xc01d265f, v25
	v_exp_f32_e32 v27, v27
	v_pk_fma_f32 v[28:29], v[138:139], s[38:39], v[10:11] op_sel_hi:[1,0,1]
	v_add_f32_e32 v27, 1.0, v27
	v_rcp_f32_e32 v27, v27
	s_nop 0
	v_mul_f32_e32 v25, v25, v27
	v_mul_f32_e32 v25, v26, v25
	v_mov_b32_e32 v26, v195
	v_cvt_pk_fp8_f32 v26, v24, v22
	v_cvt_pk_fp8_f32 v26, v23, v25 op_sel:[0,0,1]
	v_pk_fma_f32 v[24:25], v[142:143], s[38:39], v[14:15] op_sel_hi:[1,0,1]
	v_pk_fma_f32 v[22:23], v[144:145], s[38:39], v[16:17] op_sel_hi:[1,0,1]
	v_min_f32_e32 v24, 0x40e00000, v24
	v_mul_f32_e32 v30, 0xc01d265f, v24
	v_exp_f32_e32 v30, v30
	v_med3_f32 v25, v25, s23, v200
	v_min_f32_e32 v22, 0x40e00000, v22
	v_med3_f32 v23, v23, s23, v200
	v_add_f32_e32 v30, 1.0, v30
	v_rcp_f32_e32 v30, v30
	global_store_dword v[20:21], v26, off offset:64
	v_pk_fma_f32 v[26:27], v[140:141], s[38:39], v[12:13] op_sel_hi:[1,0,1]
	v_lshl_add_u64 v[20:21], v[18:19], 0, s[12:13]
; __device__ __forceinline__ unsigned pk4_fp8(float a, float b, float c, float d) { int p = 0; p = __builtin_amdgcn_cvt_pk_fp8_f32(a, b, p, false); p = __builtin_amdgcn_cvt_pk_fp8_f32(c, d, p, true); return (unsigned)p; }
;     __device__ __forceinline__ float act1(float g, float up1) const { g = fminf(g, 7.f); up1 = fminf(fmaxf(up1, -6.f), 8.f); return g * __builtin_amdgcn_rcpf(1.f + __builtin_amdgcn_exp2f(g * (-1.702f * 1.44269504f))) * up1; }
;     __device__ __forceinline__ void operator()(const f32x4 (&acc)[2][2][4][2], const Unit& u, int wr, int wc, int fr, int fq) const {
;     ...
;         for (int ai = 0; ai < 2; ++ai)
; #pragma unroll
;             for (int m = 0; m < 4; ++m) { unsigned char* rowp = ACT + (size_t)(row0 + ai * HALF + m * 16) * DFF + (col0 >> 1);
; #pragma unroll
;                 for (int bj = 0; bj < 2; ++bj) { const f32x4 v0 = acc[ai][bj][m][0] * WINV + bv[bj][0], v1 = acc[ai][bj][m][1] * WINV + bv[bj][1];
;                     *(unsigned*)(rowp + bj * (HALF / 2)) = pk4_fp8(act1(v0[0], v0[1]), act1(v0[2], v0[3]), act1(v1[0], v1[1]), act1(v1[2], v1[3])); } }
	v_mul_f32_e32 v24, v24, v30
	v_mul_f32_e32 v24, v25, v24
	v_mul_f32_e32 v25, 0xc01d265f, v22
	v_exp_f32_e32 v25, v25
	s_mov_b32 s12, 0x18000
	v_add_f32_e32 v25, 1.0, v25
	v_rcp_f32_e32 v25, v25
	s_nop 0
	v_mul_f32_e32 v22, v22, v25
	v_mul_f32_e32 v22, v23, v22
	v_min_f32_e32 v23, 0x40e00000, v28
	v_mul_f32_e32 v28, 0xc01d265f, v23
	v_exp_f32_e32 v28, v28
	v_med3_f32 v25, v29, s23, v200
	v_add_f32_e32 v28, 1.0, v28
	v_rcp_f32_e32 v28, v28
	s_nop 0
	v_mul_f32_e32 v23, v23, v28
	v_mul_f32_e32 v23, v25, v23
	v_min_f32_e32 v25, 0x40e00000, v26
	v_med3_f32 v26, v27, s23, v200
	v_mul_f32_e32 v27, 0xc01d265f, v25
	v_exp_f32_e32 v27, v27
	v_pk_fma_f32 v[28:29], v[130:131], s[38:39], v[2:3] op_sel_hi:[1,0,1]
	v_add_f32_e32 v27, 1.0, v27
	v_rcp_f32_e32 v27, v27
	s_nop 0
	v_mul_f32_e32 v25, v25, v27
	v_mul_f32_e32 v25, v26, v25
	v_mov_b32_e32 v26, v195
	v_cvt_pk_fp8_f32 v26, v24, v22
	v_add_co_u32_e32 v22, vcc, s12, v18
	s_mov_b64 s[12:13], 0x40000
	v_cvt_pk_fp8_f32 v26, v23, v25 op_sel:[0,0,1]
	v_pk_fma_f32 v[24:25], v[134:135], s[38:39], v[6:7] op_sel_hi:[1,0,1]
	v_addc_co_u32_e32 v23, vcc, 0, v19, vcc
	v_min_f32_e32 v24, 0x40e00000, v24
	v_mul_f32_e32 v30, 0xc01d265f, v24
	v_exp_f32_e32 v30, v30
	global_store_dword v[22:23], v26, off
	v_pk_fma_f32 v[22:23], v[136:137], s[38:39], v[8:9] op_sel_hi:[1,0,1]
	v_med3_f32 v25, v25, s23, v200
	v_add_f32_e32 v30, 1.0, v30
	v_rcp_f32_e32 v30, v30
	v_min_f32_e32 v22, 0x40e00000, v22
	v_med3_f32 v23, v23, s23, v200
	v_pk_fma_f32 v[26:27], v[132:133], s[38:39], v[4:5] op_sel_hi:[1,0,1]
	v_mul_f32_e32 v24, v24, v30
	v_mul_f32_e32 v24, v25, v24
	v_mul_f32_e32 v25, 0xc01d265f, v22
	v_exp_f32_e32 v25, v25
	s_nop 0
	v_add_f32_e32 v25, 1.0, v25
	v_rcp_f32_e32 v25, v25
	s_nop 0
	v_mul_f32_e32 v22, v22, v25
	v_mul_f32_e32 v22, v23, v22
	v_min_f32_e32 v23, 0x40e00000, v28
	v_mul_f32_e32 v28, 0xc01d265f, v23
	v_exp_f32_e32 v28, v28
	v_med3_f32 v25, v29, s23, v200
	v_add_f32_e32 v28, 1.0, v28
	v_rcp_f32_e32 v28, v28
	s_nop 0
	v_mul_f32_e32 v23, v23, v28
	v_mul_f32_e32 v23, v25, v23
	v_min_f32_e32 v25, 0x40e00000, v26
	v_med3_f32 v26, v27, s23, v200
	v_mul_f32_e32 v27, 0xc01d265f, v25
	v_exp_f32_e32 v27, v27
	v_pk_fma_f32 v[28:29], v[122:123], s[38:39], v[10:11] op_sel_hi:[1,0,1]
	v_add_f32_e32 v27, 1.0, v27
	v_rcp_f32_e32 v27, v27
	s_nop 0
	v_mul_f32_e32 v25, v25, v27
	v_mul_f32_e32 v25, v26, v25
	v_mov_b32_e32 v26, v195
	v_cvt_pk_fp8_f32 v26, v24, v22
	v_cvt_pk_fp8_f32 v26, v23, v25 op_sel:[0,0,1]
	v_pk_fma_f32 v[24:25], v[126:127], s[38:39], v[14:15] op_sel_hi:[1,0,1]
	v_pk_fma_f32 v[22:23], v[128:129], s[38:39], v[16:17] op_sel_hi:[1,0,1]
	v_min_f32_e32 v24, 0x40e00000, v24
	v_mul_f32_e32 v30, 0xc01d265f, v24
	v_exp_f32_e32 v30, v30
	v_med3_f32 v25, v25, s23, v200
	v_min_f32_e32 v22, 0x40e00000, v22
	v_med3_f32 v23, v23, s23, v200
	v_add_f32_e32 v30, 1.0, v30
	v_rcp_f32_e32 v30, v30
	global_store_dword v[20:21], v26, off offset:64
	v_pk_fma_f32 v[26:27], v[124:125], s[38:39], v[12:13] op_sel_hi:[1,0,1]
	v_lshl_add_u64 v[20:21], v[18:19], 0, s[12:13]
	v_mul_f32_e32 v24, v24, v30
	v_mul_f32_e32 v24, v25, v24
	v_mul_f32_e32 v25, 0xc01d265f, v22
	v_exp_f32_e32 v25, v25
	s_mov_b64 s[12:13], 0x48000
	v_add_f32_e32 v25, 1.0, v25
	v_rcp_f32_e32 v25, v25
	s_nop 0
	v_mul_f32_e32 v22, v22, v25
	v_mul_f32_e32 v22, v23, v22
	v_min_f32_e32 v23, 0x40e00000, v28
	v_mul_f32_e32 v28, 0xc01d265f, v23
	v_exp_f32_e32 v28, v28
	v_med3_f32 v25, v29, s23, v200
	v_add_f32_e32 v28, 1.0, v28
	v_rcp_f32_e32 v28, v28
	s_nop 0
	v_mul_f32_e32 v23, v23, v28
	v_mul_f32_e32 v23, v25, v23
	v_min_f32_e32 v25, 0x40e00000, v26
	v_med3_f32 v26, v27, s23, v200
	v_mul_f32_e32 v27, 0xc01d265f, v25
	v_exp_f32_e32 v27, v27
	v_pk_fma_f32 v[28:29], v[114:115], s[38:39], v[2:3] op_sel_hi:[1,0,1]
	v_add_f32_e32 v27, 1.0, v27
	v_rcp_f32_e32 v27, v27
	s_nop 0
	v_mul_f32_e32 v25, v25, v27
	v_mul_f32_e32 v25, v26, v25
	v_mov_b32_e32 v26, v195
	v_cvt_pk_fp8_f32 v26, v24, v22
	v_add_co_u32_e32 v22, vcc, s8, v18
	v_cvt_pk_fp8_f32 v26, v23, v25 op_sel:[0,0,1]
	v_pk_fma_f32 v[24:25], v[118:119], s[38:39], v[6:7] op_sel_hi:[1,0,1]
	v_addc_co_u32_e32 v23, vcc, 0, v19, vcc
	v_min_f32_e32 v24, 0x40e00000, v24
	v_mul_f32_e32 v30, 0xc01d265f, v24
	v_exp_f32_e32 v30, v30
	global_store_dword v[22:23], v26, off
	v_pk_fma_f32 v[22:23], v[120:121], s[38:39], v[8:9] op_sel_hi:[1,0,1]
	v_med3_f32 v25, v25, s23, v200
	v_add_f32_e32 v30, 1.0, v30
	v_rcp_f32_e32 v30, v30
	v_min_f32_e32 v22, 0x40e00000, v22
	v_med3_f32 v23, v23, s23, v200
	v_pk_fma_f32 v[26:27], v[116:117], s[38:39], v[4:5] op_sel_hi:[1,0,1]
	v_mul_f32_e32 v24, v24, v30
	v_mul_f32_e32 v24, v25, v24
	v_mul_f32_e32 v25, 0xc01d265f, v22
	v_exp_f32_e32 v25, v25
	s_nop 0
	v_add_f32_e32 v25, 1.0, v25
	v_rcp_f32_e32 v25, v25
	s_nop 0
	v_mul_f32_e32 v22, v22, v25
	v_mul_f32_e32 v22, v23, v22
	v_min_f32_e32 v23, 0x40e00000, v28
	v_mul_f32_e32 v28, 0xc01d265f, v23
	v_exp_f32_e32 v28, v28
	v_med3_f32 v25, v29, s23, v200
	v_add_f32_e32 v28, 1.0, v28
	v_rcp_f32_e32 v28, v28
	s_nop 0
	v_mul_f32_e32 v23, v23, v28
	v_mul_f32_e32 v23, v25, v23
	v_min_f32_e32 v25, 0x40e00000, v26
	v_med3_f32 v26, v27, s23, v200
	v_mul_f32_e32 v27, 0xc01d265f, v25
	v_exp_f32_e32 v27, v27
	v_pk_fma_f32 v[28:29], v[106:107], s[38:39], v[10:11] op_sel_hi:[1,0,1]
	v_add_f32_e32 v27, 1.0, v27
	v_rcp_f32_e32 v27, v27
	s_nop 0
	v_mul_f32_e32 v25, v25, v27
	v_mul_f32_e32 v25, v26, v25
	v_mov_b32_e32 v26, v195
	v_cvt_pk_fp8_f32 v26, v24, v22
	v_cvt_pk_fp8_f32 v26, v23, v25 op_sel:[0,0,1]
	v_pk_fma_f32 v[24:25], v[110:111], s[38:39], v[14:15] op_sel_hi:[1,0,1]
	v_pk_fma_f32 v[22:23], v[112:113], s[38:39], v[16:17] op_sel_hi:[1,0,1]
	v_min_f32_e32 v24, 0x40e00000, v24
; __device__ __forceinline__ unsigned pk4_fp8(float a, float b, float c, float d) { int p = 0; p = __builtin_amdgcn_cvt_pk_fp8_f32(a, b, p, false); p = __builtin_amdgcn_cvt_pk_fp8_f32(c, d, p, true); return (unsigned)p; }
;     __device__ __forceinline__ float act1(float g, float up1) const { g = fminf(g, 7.f); up1 = fminf(fmaxf(up1, -6.f), 8.f); return g * __builtin_amdgcn_rcpf(1.f + __builtin_amdgcn_exp2f(g * (-1.702f * 1.44269504f))) * up1; }
;     __device__ __forceinline__ void operator()(const f32x4 (&acc)[2][2][4][2], const Unit& u, int wr, int wc, int fr, int fq) const {
;     ...
;         for (int ai = 0; ai < 2; ++ai)
; #pragma unroll
;             for (int m = 0; m < 4; ++m) { unsigned char* rowp = ACT + (size_t)(row0 + ai * HALF + m * 16) * DFF + (col0 >> 1);
; #pragma unroll
;                 for (int bj = 0; bj < 2; ++bj) { const f32x4 v0 = acc[ai][bj][m][0] * WINV + bv[bj][0], v1 = acc[ai][bj][m][1] * WINV + bv[bj][1];
;                     *(unsigned*)(rowp + bj * (HALF / 2)) = pk4_fp8(act1(v0[0], v0[1]), act1(v0[2], v0[3]), act1(v1[0], v1[1]), act1(v1[2], v1[3])); } }
	v_mul_f32_e32 v30, 0xc01d265f, v24
	v_exp_f32_e32 v30, v30
	v_med3_f32 v25, v25, s23, v200
	v_min_f32_e32 v22, 0x40e00000, v22
	v_med3_f32 v23, v23, s23, v200
	v_add_f32_e32 v30, 1.0, v30
	v_rcp_f32_e32 v30, v30
	global_store_dword v[20:21], v26, off offset:64
	v_pk_fma_f32 v[26:27], v[108:109], s[38:39], v[12:13] op_sel_hi:[1,0,1]
	v_lshl_add_u64 v[20:21], v[18:19], 0, s[12:13]
	v_mul_f32_e32 v24, v24, v30
	v_mul_f32_e32 v24, v25, v24
	v_mul_f32_e32 v25, 0xc01d265f, v22
	v_exp_f32_e32 v25, v25
	s_mov_b32 s12, 0x48000
	v_add_f32_e32 v25, 1.0, v25
	v_rcp_f32_e32 v25, v25
	s_nop 0
	v_mul_f32_e32 v22, v22, v25
	v_mul_f32_e32 v22, v23, v22
	v_min_f32_e32 v23, 0x40e00000, v28
	v_mul_f32_e32 v28, 0xc01d265f, v23
	v_exp_f32_e32 v28, v28
	v_med3_f32 v25, v29, s23, v200
	v_add_f32_e32 v28, 1.0, v28
	v_rcp_f32_e32 v28, v28
	s_nop 0
	v_mul_f32_e32 v23, v23, v28
	v_mul_f32_e32 v23, v25, v23
	v_min_f32_e32 v25, 0x40e00000, v26
	v_med3_f32 v26, v27, s23, v200
	v_mul_f32_e32 v27, 0xc01d265f, v25
	v_exp_f32_e32 v27, v27
	v_pk_fma_f32 v[28:29], v[98:99], s[38:39], v[2:3] op_sel_hi:[1,0,1]
	v_add_f32_e32 v27, 1.0, v27
	v_rcp_f32_e32 v27, v27
	s_nop 0
	v_mul_f32_e32 v25, v25, v27
	v_mul_f32_e32 v25, v26, v25
	v_mov_b32_e32 v26, v195
	v_cvt_pk_fp8_f32 v26, v24, v22
	v_add_co_u32_e32 v22, vcc, s12, v18
	s_mov_b64 s[12:13], 0x50000
	v_cvt_pk_fp8_f32 v26, v23, v25 op_sel:[0,0,1]
	v_pk_fma_f32 v[24:25], v[102:103], s[38:39], v[6:7] op_sel_hi:[1,0,1]
	v_addc_co_u32_e32 v23, vcc, 0, v19, vcc
	v_min_f32_e32 v24, 0x40e00000, v24
	v_mul_f32_e32 v30, 0xc01d265f, v24
	v_exp_f32_e32 v30, v30
	global_store_dword v[22:23], v26, off
	v_pk_fma_f32 v[22:23], v[104:105], s[38:39], v[8:9] op_sel_hi:[1,0,1]
	v_med3_f32 v25, v25, s23, v200
	v_add_f32_e32 v30, 1.0, v30
	v_rcp_f32_e32 v30, v30
	v_min_f32_e32 v22, 0x40e00000, v22
	v_med3_f32 v23, v23, s23, v200
	v_pk_fma_f32 v[26:27], v[100:101], s[38:39], v[4:5] op_sel_hi:[1,0,1]
	v_mul_f32_e32 v24, v24, v30
	v_mul_f32_e32 v24, v25, v24
	v_mul_f32_e32 v25, 0xc01d265f, v22
	v_exp_f32_e32 v25, v25
	s_nop 0
	v_add_f32_e32 v25, 1.0, v25
	v_rcp_f32_e32 v25, v25
	s_nop 0
	v_mul_f32_e32 v22, v22, v25
	v_mul_f32_e32 v22, v23, v22
	v_min_f32_e32 v23, 0x40e00000, v28
	v_mul_f32_e32 v28, 0xc01d265f, v23
	v_exp_f32_e32 v28, v28
	v_med3_f32 v25, v29, s23, v200
	v_add_f32_e32 v28, 1.0, v28
	v_rcp_f32_e32 v28, v28
	s_nop 0
	v_mul_f32_e32 v23, v23, v28
	v_mul_f32_e32 v23, v25, v23
	v_min_f32_e32 v25, 0x40e00000, v26
	v_med3_f32 v26, v27, s23, v200
	v_mul_f32_e32 v27, 0xc01d265f, v25
	v_exp_f32_e32 v27, v27
	v_pk_fma_f32 v[28:29], v[90:91], s[38:39], v[10:11] op_sel_hi:[1,0,1]
	v_pk_fma_f32 v[10:11], v[74:75], s[38:39], v[10:11] op_sel_hi:[1,0,1]
	v_add_f32_e32 v27, 1.0, v27
	v_rcp_f32_e32 v27, v27
	v_min_f32_e32 v10, 0x40e00000, v10
	v_med3_f32 v11, v11, s23, v200
	v_mul_f32_e32 v25, v25, v27
	v_mul_f32_e32 v25, v26, v25
	v_mov_b32_e32 v26, v195
	v_cvt_pk_fp8_f32 v26, v24, v22
	v_cvt_pk_fp8_f32 v26, v23, v25 op_sel:[0,0,1]
	v_pk_fma_f32 v[24:25], v[94:95], s[38:39], v[14:15] op_sel_hi:[1,0,1]
	v_pk_fma_f32 v[22:23], v[96:97], s[38:39], v[16:17] op_sel_hi:[1,0,1]
	v_min_f32_e32 v24, 0x40e00000, v24
	v_mul_f32_e32 v30, 0xc01d265f, v24
	v_exp_f32_e32 v30, v30
	v_med3_f32 v25, v25, s23, v200
	v_min_f32_e32 v22, 0x40e00000, v22
	v_med3_f32 v23, v23, s23, v200
	v_add_f32_e32 v30, 1.0, v30
	v_rcp_f32_e32 v30, v30
	global_store_dword v[20:21], v26, off offset:64
	v_pk_fma_f32 v[26:27], v[92:93], s[38:39], v[12:13] op_sel_hi:[1,0,1]
	v_lshl_add_u64 v[20:21], v[18:19], 0, s[12:13]
	v_mul_f32_e32 v24, v24, v30
	v_mul_f32_e32 v24, v25, v24
	v_mul_f32_e32 v25, 0xc01d265f, v22
	v_exp_f32_e32 v25, v25
	s_mov_b32 s12, 0x50000
	v_pk_fma_f32 v[14:15], v[78:79], s[38:39], v[14:15] op_sel_hi:[1,0,1]
	v_pk_fma_f32 v[16:17], v[80:81], s[38:39], v[16:17] op_sel_hi:[1,0,1]
	v_add_f32_e32 v25, 1.0, v25
	v_rcp_f32_e32 v25, v25
	v_min_f32_e32 v14, 0x40e00000, v14
	v_med3_f32 v15, v15, s23, v200
	v_pk_fma_f32 v[12:13], v[76:77], s[38:39], v[12:13] op_sel_hi:[1,0,1]
	v_mul_f32_e32 v22, v22, v25
	v_mul_f32_e32 v22, v23, v22
	v_min_f32_e32 v23, 0x40e00000, v28
	v_mul_f32_e32 v28, 0xc01d265f, v23
	v_exp_f32_e32 v28, v28
	v_med3_f32 v25, v29, s23, v200
	v_add_f32_e32 v28, 1.0, v28
	v_rcp_f32_e32 v28, v28
	s_nop 0
	v_mul_f32_e32 v23, v23, v28
	v_mul_f32_e32 v23, v25, v23
	v_min_f32_e32 v25, 0x40e00000, v26
	v_med3_f32 v26, v27, s23, v200
	v_mul_f32_e32 v27, 0xc01d265f, v25
	v_exp_f32_e32 v27, v27
; __device__ __forceinline__ unsigned pk4_fp8(float a, float b, float c, float d) { int p = 0; p = __builtin_amdgcn_cvt_pk_fp8_f32(a, b, p, false); p = __builtin_amdgcn_cvt_pk_fp8_f32(c, d, p, true); return (unsigned)p; }
;     __device__ __forceinline__ float act1(float g, float up1) const { g = fminf(g, 7.f); up1 = fminf(fmaxf(up1, -6.f), 8.f); return g * __builtin_amdgcn_rcpf(1.f + __builtin_amdgcn_exp2f(g * (-1.702f * 1.44269504f))) * up1; }
; #define PG8_BAR __builtin_amdgcn_s_barrier()
;     __device__ __forceinline__ void operator()(const f32x4 (&acc)[2][2][4][2], const Unit& u, int wr, int wc, int fr, int fq) const {
;     ...
;         for (int ai = 0; ai < 2; ++ai)
; #pragma unroll
;             for (int m = 0; m < 4; ++m) { unsigned char* rowp = ACT + (size_t)(row0 + ai * HALF + m * 16) * DFF + (col0 >> 1);
; #pragma unroll
;                 for (int bj = 0; bj < 2; ++bj) { const f32x4 v0 = acc[ai][bj][m][0] * WINV + bv[bj][0], v1 = acc[ai][bj][m][1] * WINV + bv[bj][1];
;                     *(unsigned*)(rowp + bj * (HALF / 2)) = pk4_fp8(act1(v0[0], v0[1]), act1(v0[2], v0[3]), act1(v1[0], v1[1]), act1(v1[2], v1[3])); } }
; template <class Epi, class Sched>
; __device__ __forceinline__ void gemm_phase(LAS unsigned char* lds, const Sched& S, const Epi& E) {
;     ...
;         if (!has_next) break;
; #pragma unroll
;         for (int a = 0; a < 2; ++a)
; #pragma unroll
;             for (int b = 0; b < 2; ++b)
; #pragma unroll
;                 for (int m = 0; m < 4; ++m)
; #pragma unroll
;                     for (int n = 0; n < 2; ++n) acc[a][b][m][n] = (f32x4){0.f, 0.f, 0.f, 0.f};
;         cur = nxt; cA = nA; cB = nB; ++ui;
;         if (wr == 1) PG8_BAR;
	v_pk_fma_f32 v[28:29], v[82:83], s[38:39], v[2:3] op_sel_hi:[1,0,1]
	v_pk_fma_f32 v[2:3], v[66:67], s[38:39], v[2:3] op_sel_hi:[1,0,1]
	v_add_f32_e32 v27, 1.0, v27
	v_rcp_f32_e32 v27, v27
	v_min_f32_e32 v2, 0x40e00000, v2
	v_med3_f32 v3, v3, s23, v200
	v_mul_f32_e32 v25, v25, v27
	v_mul_f32_e32 v25, v26, v25
	v_mov_b32_e32 v26, v195
	v_cvt_pk_fp8_f32 v26, v24, v22
	v_add_co_u32_e32 v22, vcc, s12, v18
	s_mov_b64 s[12:13], 0x58000
	v_cvt_pk_fp8_f32 v26, v23, v25 op_sel:[0,0,1]
	v_pk_fma_f32 v[24:25], v[86:87], s[38:39], v[6:7] op_sel_hi:[1,0,1]
	v_addc_co_u32_e32 v23, vcc, 0, v19, vcc
	v_min_f32_e32 v24, 0x40e00000, v24
	v_mul_f32_e32 v30, 0xc01d265f, v24
	v_exp_f32_e32 v30, v30
	global_store_dword v[22:23], v26, off
	v_pk_fma_f32 v[22:23], v[88:89], s[38:39], v[8:9] op_sel_hi:[1,0,1]
	v_med3_f32 v25, v25, s23, v200
	v_add_f32_e32 v30, 1.0, v30
	v_rcp_f32_e32 v30, v30
	v_min_f32_e32 v22, 0x40e00000, v22
	v_med3_f32 v23, v23, s23, v200
	v_pk_fma_f32 v[26:27], v[84:85], s[38:39], v[4:5] op_sel_hi:[1,0,1]
	v_mul_f32_e32 v24, v24, v30
	v_mul_f32_e32 v24, v25, v24
	v_mul_f32_e32 v25, 0xc01d265f, v22
	v_exp_f32_e32 v25, v25
	v_pk_fma_f32 v[6:7], v[70:71], s[38:39], v[6:7] op_sel_hi:[1,0,1]
	v_pk_fma_f32 v[8:9], v[72:73], s[38:39], v[8:9] op_sel_hi:[1,0,1]
	v_min_f32_e32 v6, 0x40e00000, v6
	v_add_f32_e32 v25, 1.0, v25
	v_rcp_f32_e32 v25, v25
	v_med3_f32 v7, v7, s23, v200
	v_pk_fma_f32 v[4:5], v[68:69], s[38:39], v[4:5] op_sel_hi:[1,0,1]
	v_mul_f32_e32 v22, v22, v25
	v_mul_f32_e32 v22, v23, v22
	v_min_f32_e32 v23, 0x40e00000, v28
	v_mul_f32_e32 v28, 0xc01d265f, v23
	v_exp_f32_e32 v28, v28
	v_med3_f32 v25, v29, s23, v200
	v_add_f32_e32 v28, 1.0, v28
	v_rcp_f32_e32 v28, v28
	s_nop 0
	v_mul_f32_e32 v23, v23, v28
	v_mul_f32_e32 v23, v25, v23
	v_min_f32_e32 v25, 0x40e00000, v26
	v_med3_f32 v26, v27, s23, v200
	v_mul_f32_e32 v27, 0xc01d265f, v25
	v_exp_f32_e32 v27, v27
	s_nop 0
	v_add_f32_e32 v27, 1.0, v27
	v_rcp_f32_e32 v27, v27
	s_nop 0
	v_mul_f32_e32 v25, v25, v27
	v_mul_f32_e32 v25, v26, v25
	v_mov_b32_e32 v26, v195
	v_cvt_pk_fp8_f32 v26, v24, v22
	v_mul_f32_e32 v22, 0xc01d265f, v14
	v_exp_f32_e32 v22, v22
	v_cvt_pk_fp8_f32 v26, v23, v25 op_sel:[0,0,1]
	v_add_f32_e32 v22, 1.0, v22
	v_rcp_f32_e32 v22, v22
	global_store_dword v[20:21], v26, off offset:64
	v_lshl_add_u64 v[20:21], v[18:19], 0, s[12:13]
	s_mov_b32 s12, 0x58000
	v_mul_f32_e32 v14, v14, v22
	v_mul_f32_e32 v14, v15, v14
	v_min_f32_e32 v15, 0x40e00000, v16
	v_med3_f32 v16, v17, s23, v200
	v_mul_f32_e32 v17, 0xc01d265f, v15
	v_exp_f32_e32 v17, v17
	s_nop 0
	v_add_f32_e32 v17, 1.0, v17
	v_rcp_f32_e32 v17, v17
	s_nop 0
	v_mul_f32_e32 v15, v15, v17
	v_mul_f32_e32 v15, v16, v15
	v_mul_f32_e32 v16, 0xc01d265f, v10
	v_exp_f32_e32 v16, v16
	s_nop 0
	v_add_f32_e32 v16, 1.0, v16
	v_rcp_f32_e32 v16, v16
	s_nop 0
	v_mul_f32_e32 v10, v10, v16
	v_mul_f32_e32 v10, v11, v10
	v_min_f32_e32 v11, 0x40e00000, v12
	v_med3_f32 v12, v13, s23, v200
	v_mul_f32_e32 v13, 0xc01d265f, v11
	v_exp_f32_e32 v13, v13
	s_nop 0
	v_add_f32_e32 v13, 1.0, v13
	v_rcp_f32_e32 v13, v13
	s_nop 0
	v_mul_f32_e32 v11, v11, v13
	v_mul_f32_e32 v11, v12, v11
	v_mov_b32_e32 v12, v195
	v_cvt_pk_fp8_f32 v12, v14, v15
	v_cvt_pk_fp8_f32 v12, v10, v11 op_sel:[0,0,1]
	v_add_co_u32_e32 v10, vcc, s12, v18
	s_nop 1
	v_addc_co_u32_e32 v11, vcc, 0, v19, vcc
	global_store_dword v[10:11], v12, off
	v_mul_f32_e32 v10, 0xc01d265f, v6
	v_exp_f32_e32 v10, v10
	s_and_b64 vcc, exec, s[2:3]
	v_add_f32_e32 v10, 1.0, v10
	v_rcp_f32_e32 v10, v10
	s_nop 0
	v_mul_f32_e32 v6, v6, v10
	v_mul_f32_e32 v6, v7, v6
	v_min_f32_e32 v7, 0x40e00000, v8
	v_med3_f32 v8, v9, s23, v200
	v_mul_f32_e32 v9, 0xc01d265f, v7
	v_exp_f32_e32 v9, v9
	s_nop 0
	v_add_f32_e32 v9, 1.0, v9
	v_rcp_f32_e32 v9, v9
	s_nop 0
	v_mul_f32_e32 v7, v7, v9
	v_mul_f32_e32 v7, v8, v7
	v_mul_f32_e32 v8, 0xc01d265f, v2
	v_exp_f32_e32 v8, v8
	s_nop 0
	v_add_f32_e32 v8, 1.0, v8
	v_rcp_f32_e32 v8, v8
	s_nop 0
	v_mul_f32_e32 v2, v2, v8
	v_mul_f32_e32 v2, v3, v2
	v_min_f32_e32 v3, 0x40e00000, v4
	v_med3_f32 v4, v5, s23, v200
	v_mul_f32_e32 v5, 0xc01d265f, v3
	v_exp_f32_e32 v5, v5
	s_nop 0
	v_add_f32_e32 v5, 1.0, v5
	v_rcp_f32_e32 v5, v5
	s_nop 0
	v_mul_f32_e32 v3, v3, v5
	v_mul_f32_e32 v3, v4, v3
	v_mov_b32_e32 v4, v195
	v_cvt_pk_fp8_f32 v4, v6, v7
	v_cvt_pk_fp8_f32 v4, v2, v3 op_sel:[0,0,1]
	global_store_dword v[20:21], v4, off offset:64
	s_cbranch_vccnz .LBB0_1001
	s_andn2_b64 vcc, exec, s[0:1]
	s_cbranch_vccnz .LBB0_1000
	s_barrier
	s_branch .LBB0_1000

;     __device__ __forceinline__ const char* a_base(const Unit& u) const { return GATHER ? A : A + ((size_t)__builtin_amdgcn_readfirstlane(poff[u.e]) + (size_t)u.pm * BM) * ROWB; }
;     __device__ __forceinline__ void operator()(const f32x4 (&acc)[2][2][4][2], const Unit& u, int wr, int wc, int fr, int fq) const {
;         const int row0 = poff[u.e] + u.pm * BM + wr * 64 + fr, col0 = u.pn * BM + wc * 32 + 8 * fq;
;         const float* bp = bias + (size_t)u.e * D + col0;
; #pragma unroll
;         for (int bj = 0; bj < 2; ++bj) { const f32x4 b0 = *(const f32x4*)(bp + bj * HALF), b1 = *(const f32x4*)(bp + bj * HALF + 4);
; template <class Epi, class Sched>
; __device__ __forceinline__ void gemm_phase(LAS unsigned char* lds, const Sched& S, const Epi& E) {
;     ...
;     for (;;) {
;         const bool has_next = S.next(ui + 1, nxt);
;         const char* nA = has_next ? S.a_base(nxt) : cA; const char* nB = has_next ? S.b_base(nxt) : cB;
;         if (has_next) S.idx_prefetch(nxt, ldsb + IDX_OFF, wid, lane);
.LBB0_1456:
	v_readlane_b32 s98, v253, 0
	s_lshr_b32 s98, s98, 6
	s_cmp_lg_u32 s98, 7
	s_cbranch_scc1 .Lbp8_skip
	s_lshl_b32 s98, s40, 13
	s_lshl_b32 s99, s84, 10
	s_add_i32 s98, s98, s99
	s_add_u32 s98, s68, s98
	s_addc_u32 s99, s69, 0
	s_and_b32 s100, s62, 1
	s_lshl_b32 s100, s100, 10
	s_add_i32 s100, s100, 0x23000
	v_mbcnt_lo_u32_b32 v255, -1, 0
	v_mbcnt_hi_u32_b32 v255, -1, v255
	v_lshlrev_b32_e32 v255, 4, v255
	s_mov_b32 s101, m0
	s_mov_b32 m0, s100
	s_nop 0
	global_load_lds_dwordx4 v255, s[98:99]
	s_mov_b32 m0, s101

; __device__ __forceinline__ unsigned pk4_fp8(float a, float b, float c, float d) { int p = 0; p = __builtin_amdgcn_cvt_pk_fp8_f32(a, b, p, false); p = __builtin_amdgcn_cvt_pk_fp8_f32(c, d, p, true); return (unsigned)p; }
;     __device__ __forceinline__ void operator()(const f32x4 (&acc)[2][2][4][2], const Unit& u, int wr, int wc, int fr, int fq) const {
;         const int row0 = poff[u.e] + u.pm * BM + wr * 64 + fr, col0 = u.pn * BM + wc * 32 + 8 * fq;
;         const float* bp = bias + (size_t)u.e * D + col0;
; #pragma unroll
;         for (int bj = 0; bj < 2; ++bj) { const f32x4 b0 = *(const f32x4*)(bp + bj * HALF), b1 = *(const f32x4*)(bp + bj * HALF + 4);
; #pragma unroll
;             for (int ai = 0; ai < 2; ++ai)
; #pragma unroll
;                 for (int m = 0; m < 4; ++m) { unsigned char* rowp = YS + (size_t)(row0 + ai * HALF + m * 16) * D + col0 + bj * HALF;
;                     const f32x4 v0 = (acc[ai][bj][m][0] * WINV + b0) * YSCALE, v1 = (acc[ai][bj][m][1] * WINV + b1) * YSCALE;
;                     u32x2 w; w.x = pk4_fp8(v0[0], v0[1], v0[2], v0[3]); w.y = pk4_fp8(v1[0], v1[1], v1[2], v1[3]);
;                     *(u32x2*)rowp = w; } }
.LBB0_1467:
	s_lshl_b32 s27, s40, 2
	s_add_i32 s27, s27, 0
	s_add_i32 s27, s27, 0x20300
	v_mov_b32_e32 v122, v1
	v_mov_b32_e32 v123, s27
	s_ashr_i32 s41, s40, 31
	ds_read_b32 v123, v123
	s_lshl_b32 s29, s84, 8
	v_ashrrev_i32_e32 v124, 1, v122
	s_lshl_b32 s27, s42, 8
	v_and_b32_e32 v124, -8, v124
	s_or_b32 s29, s29, s8
	s_lshl_b64 s[40:41], s[40:41], 13
	v_add_u32_e32 v142, s29, v124
	s_add_u32 s40, s68, s40
	s_addc_u32 s41, s69, s41
	v_ashrrev_i32_e32 v143, 31, v142
	s_add_i32 s27, s27, s78
	s_and_b32 s100, s62, 1
	s_xor_b32 s100, s100, 1
	s_lshl_b32 s100, s100, 10
	s_add_i32 s100, s100, 0x23000
	v_and_b32_e32 v144, 0xff, v142
	v_lshlrev_b32_e32 v144, 2, v144
	v_add_u32_e32 v144, s100, v144
	v_and_or_b32 v122, v122, 15, s27
	s_waitcnt lgkmcnt(0)
	v_add_u32_e32 v156, v122, v123
	ds_read_b128 v[122:125], v144 offset:16
	ds_read_b128 v[134:137], v144
	ds_read_b128 v[160:163], v144 offset:528
	ds_read_b128 v[164:167], v144 offset:512
	v_ashrrev_i32_e32 v157, 31, v156
	v_lshlrev_b64 v[156:157], 11, v[156:157]
	v_lshl_add_u64 v[156:157], s[6:7], 0, v[156:157]
	v_lshl_add_u64 v[142:143], v[156:157], 0, v[142:143]
	v_mov_b32_e32 v157, v139
	s_mov_b32 s27, 0x8000
	v_mov_b32_e32 v156, v139
	s_mov_b64 s[40:41], 0x8000
	s_waitcnt lgkmcnt(3)
	v_pk_fma_f32 v[126:127], v[126:127], s[18:19], v[122:123] op_sel_hi:[1,0,1]
	s_nop 0
	v_pk_mul_f32 v[126:127], v[126:127], s[20:21] op_sel_hi:[1,0]
	v_pk_fma_f32 v[128:129], v[128:129], s[18:19], v[124:125] op_sel_hi:[1,0,1]
	v_cvt_pk_fp8_f32 v157, v126, v127
	v_pk_mul_f32 v[128:129], v[128:129], s[20:21] op_sel_hi:[1,0]
	v_pk_fma_f32 v[114:115], v[114:115], s[18:19], v[122:123] op_sel_hi:[1,0,1]
	v_pk_fma_f32 v[116:117], v[116:117], s[18:19], v[124:125] op_sel_hi:[1,0,1]
	v_cvt_pk_fp8_f32 v157, v128, v129 op_sel:[0,0,1]
	v_pk_mul_f32 v[114:115], v[114:115], s[20:21] op_sel_hi:[1,0]
	v_mov_b32_e32 v129, v139
	v_cvt_pk_fp8_f32 v129, v114, v115
	v_pk_mul_f32 v[116:117], v[116:117], s[20:21] op_sel_hi:[1,0]
	v_pk_fma_f32 v[106:107], v[106:107], s[18:19], v[122:123] op_sel_hi:[1,0,1]
	v_pk_fma_f32 v[108:109], v[108:109], s[18:19], v[124:125] op_sel_hi:[1,0,1]
	v_cvt_pk_fp8_f32 v129, v116, v117 op_sel:[0,0,1]
	v_pk_mul_f32 v[106:107], v[106:107], s[20:21] op_sel_hi:[1,0]
	v_mov_b32_e32 v117, v139
	v_cvt_pk_fp8_f32 v117, v106, v107
	v_pk_mul_f32 v[108:109], v[108:109], s[20:21] op_sel_hi:[1,0]
	s_waitcnt lgkmcnt(2)
	v_pk_fma_f32 v[102:103], v[102:103], s[18:19], v[134:135] op_sel_hi:[1,0,1]
	v_pk_fma_f32 v[98:99], v[98:99], s[18:19], v[122:123] op_sel_hi:[1,0,1]
	v_cvt_pk_fp8_f32 v117, v108, v109 op_sel:[0,0,1]
	v_pk_mul_f32 v[102:103], v[102:103], s[20:21] op_sel_hi:[1,0]
	v_pk_mul_f32 v[108:109], v[98:99], s[20:21] op_sel_hi:[1,0]
	v_mov_b32_e32 v98, v139
	v_mov_b32_e32 v99, v139
	v_cvt_pk_fp8_f32 v98, v102, v103
	v_cvt_pk_fp8_f32 v99, v108, v109
	v_add_co_u32_e32 v114, vcc, s27, v142
	v_pk_fma_f32 v[104:105], v[104:105], s[18:19], v[136:137] op_sel_hi:[1,0,1]
	v_pk_fma_f32 v[100:101], v[100:101], s[18:19], v[124:125] op_sel_hi:[1,0,1]
	v_addc_co_u32_e32 v115, vcc, 0, v143, vcc
	s_mov_b32 s27, 0x10000
	v_pk_mul_f32 v[104:105], v[104:105], s[20:21] op_sel_hi:[1,0]
	v_pk_mul_f32 v[100:101], v[100:101], s[20:21] op_sel_hi:[1,0]
	v_add_co_u32_e32 v106, vcc, s27, v142
	v_cvt_pk_fp8_f32 v98, v104, v105 op_sel:[0,0,1]
	v_cvt_pk_fp8_f32 v99, v100, v101 op_sel:[0,0,1]
	v_addc_co_u32_e32 v107, vcc, 0, v143, vcc
	s_mov_b32 s27, 0x18000
	v_add_co_u32_e32 v100, vcc, s27, v142
	v_pk_fma_f32 v[90:91], v[90:91], s[18:19], v[122:123] op_sel_hi:[1,0,1]
	s_nop 0
	v_addc_co_u32_e32 v101, vcc, 0, v143, vcc
	global_store_dwordx2 v[100:101], v[98:99], off
	v_pk_mul_f32 v[90:91], v[90:91], s[20:21] op_sel_hi:[1,0]
	v_mov_b32_e32 v101, v139
	v_cvt_pk_fp8_f32 v101, v90, v91
	v_pk_fma_f32 v[92:93], v[92:93], s[18:19], v[124:125] op_sel_hi:[1,0,1]
	v_pk_fma_f32 v[82:83], v[82:83], s[18:19], v[122:123] op_sel_hi:[1,0,1]
	v_pk_mul_f32 v[92:93], v[92:93], s[20:21] op_sel_hi:[1,0]
	v_pk_mul_f32 v[82:83], v[82:83], s[20:21] op_sel_hi:[1,0]
	v_cvt_pk_fp8_f32 v101, v92, v93 op_sel:[0,0,1]
	v_mov_b32_e32 v93, v139
	v_cvt_pk_fp8_f32 v93, v82, v83
	v_pk_fma_f32 v[84:85], v[84:85], s[18:19], v[124:125] op_sel_hi:[1,0,1]
	v_pk_fma_f32 v[74:75], v[74:75], s[18:19], v[122:123] op_sel_hi:[1,0,1]
	v_pk_mul_f32 v[84:85], v[84:85], s[20:21] op_sel_hi:[1,0]
	v_pk_mul_f32 v[74:75], v[74:75], s[20:21] op_sel_hi:[1,0]
	v_cvt_pk_fp8_f32 v93, v84, v85 op_sel:[0,0,1]
	v_mov_b32_e32 v85, v139
	v_cvt_pk_fp8_f32 v85, v74, v75
	v_pk_fma_f32 v[76:77], v[76:77], s[18:19], v[124:125] op_sel_hi:[1,0,1]
	v_pk_fma_f32 v[130:131], v[130:131], s[18:19], v[134:135] op_sel_hi:[1,0,1]
	v_pk_fma_f32 v[118:119], v[118:119], s[18:19], v[134:135] op_sel_hi:[1,0,1]
	v_pk_fma_f32 v[110:111], v[110:111], s[18:19], v[134:135] op_sel_hi:[1,0,1]
	v_pk_fma_f32 v[94:95], v[94:95], s[18:19], v[134:135] op_sel_hi:[1,0,1]
	v_pk_fma_f32 v[86:87], v[86:87], s[18:19], v[134:135] op_sel_hi:[1,0,1]
	v_pk_fma_f32 v[78:79], v[78:79], s[18:19], v[134:135] op_sel_hi:[1,0,1]
	v_pk_mul_f32 v[76:77], v[76:77], s[20:21] op_sel_hi:[1,0]
	v_pk_fma_f32 v[70:71], v[70:71], s[18:19], v[134:135] op_sel_hi:[1,0,1]
	v_pk_fma_f32 v[66:67], v[66:67], s[18:19], v[122:123] op_sel_hi:[1,0,1]
	v_pk_mul_f32 v[130:131], v[130:131], s[20:21] op_sel_hi:[1,0]
	v_pk_mul_f32 v[118:119], v[118:119], s[20:21] op_sel_hi:[1,0]
	v_mov_b32_e32 v128, v139
	v_pk_mul_f32 v[110:111], v[110:111], s[20:21] op_sel_hi:[1,0]
	v_mov_b32_e32 v116, v139
	v_pk_mul_f32 v[94:95], v[94:95], s[20:21] op_sel_hi:[1,0]
	v_mov_b32_e32 v100, v139
	s_mov_b32 s27, 0x40000
	v_pk_mul_f32 v[86:87], v[86:87], s[20:21] op_sel_hi:[1,0]
	v_mov_b32_e32 v92, v139
; __device__ __forceinline__ unsigned pk4_fp8(float a, float b, float c, float d) { int p = 0; p = __builtin_amdgcn_cvt_pk_fp8_f32(a, b, p, false); p = __builtin_amdgcn_cvt_pk_fp8_f32(c, d, p, true); return (unsigned)p; }
;     __device__ __forceinline__ void operator()(const f32x4 (&acc)[2][2][4][2], const Unit& u, int wr, int wc, int fr, int fq) const {
;         const int row0 = poff[u.e] + u.pm * BM + wr * 64 + fr, col0 = u.pn * BM + wc * 32 + 8 * fq;
;         const float* bp = bias + (size_t)u.e * D + col0;
; #pragma unroll
;         for (int bj = 0; bj < 2; ++bj) { const f32x4 b0 = *(const f32x4*)(bp + bj * HALF), b1 = *(const f32x4*)(bp + bj * HALF + 4);
; #pragma unroll
;             for (int ai = 0; ai < 2; ++ai)
; #pragma unroll
;                 for (int m = 0; m < 4; ++m) { unsigned char* rowp = YS + (size_t)(row0 + ai * HALF + m * 16) * D + col0 + bj * HALF;
;                     const f32x4 v0 = (acc[ai][bj][m][0] * WINV + b0) * YSCALE, v1 = (acc[ai][bj][m][1] * WINV + b1) * YSCALE;
;                     u32x2 w; w.x = pk4_fp8(v0[0], v0[1], v0[2], v0[3]); w.y = pk4_fp8(v1[0], v1[1], v1[2], v1[3]);
;                     *(u32x2*)rowp = w; } }
	v_pk_mul_f32 v[78:79], v[78:79], s[20:21] op_sel_hi:[1,0]
	v_mov_b32_e32 v84, v139
	v_cvt_pk_fp8_f32 v85, v76, v77 op_sel:[0,0,1]
	v_pk_mul_f32 v[70:71], v[70:71], s[20:21] op_sel_hi:[1,0]
	v_pk_mul_f32 v[66:67], v[66:67], s[20:21] op_sel_hi:[1,0]
	v_mov_b32_e32 v76, v139
	v_mov_b32_e32 v77, v139
	v_cvt_pk_fp8_f32 v156, v130, v131
	v_cvt_pk_fp8_f32 v128, v118, v119
	v_cvt_pk_fp8_f32 v116, v110, v111
	v_cvt_pk_fp8_f32 v100, v94, v95
	v_add_co_u32_e32 v90, vcc, s27, v142
	v_cvt_pk_fp8_f32 v92, v86, v87
	v_cvt_pk_fp8_f32 v84, v78, v79
	v_cvt_pk_fp8_f32 v76, v70, v71
	v_cvt_pk_fp8_f32 v77, v66, v67
	v_addc_co_u32_e32 v91, vcc, 0, v143, vcc
	s_mov_b32 s27, 0x48000
	v_pk_fma_f32 v[132:133], v[132:133], s[18:19], v[136:137] op_sel_hi:[1,0,1]
	v_pk_fma_f32 v[120:121], v[120:121], s[18:19], v[136:137] op_sel_hi:[1,0,1]
	v_pk_fma_f32 v[112:113], v[112:113], s[18:19], v[136:137] op_sel_hi:[1,0,1]
	v_pk_fma_f32 v[96:97], v[96:97], s[18:19], v[136:137] op_sel_hi:[1,0,1]
	v_pk_fma_f32 v[88:89], v[88:89], s[18:19], v[136:137] op_sel_hi:[1,0,1]
	v_add_co_u32_e32 v82, vcc, s27, v142
	v_pk_fma_f32 v[80:81], v[80:81], s[18:19], v[136:137] op_sel_hi:[1,0,1]
	v_pk_fma_f32 v[72:73], v[72:73], s[18:19], v[136:137] op_sel_hi:[1,0,1]
	v_pk_fma_f32 v[68:69], v[68:69], s[18:19], v[124:125] op_sel_hi:[1,0,1]
	v_pk_mul_f32 v[132:133], v[132:133], s[20:21] op_sel_hi:[1,0]
	v_pk_mul_f32 v[120:121], v[120:121], s[20:21] op_sel_hi:[1,0]
	v_pk_mul_f32 v[112:113], v[112:113], s[20:21] op_sel_hi:[1,0]
	v_pk_mul_f32 v[96:97], v[96:97], s[20:21] op_sel_hi:[1,0]
	v_pk_mul_f32 v[88:89], v[88:89], s[20:21] op_sel_hi:[1,0]
	v_addc_co_u32_e32 v83, vcc, 0, v143, vcc
	v_pk_mul_f32 v[80:81], v[80:81], s[20:21] op_sel_hi:[1,0]
	s_mov_b32 s27, 0x50000
	v_pk_mul_f32 v[72:73], v[72:73], s[20:21] op_sel_hi:[1,0]
	v_pk_mul_f32 v[68:69], v[68:69], s[20:21] op_sel_hi:[1,0]
	v_cvt_pk_fp8_f32 v156, v132, v133 op_sel:[0,0,1]
	v_cvt_pk_fp8_f32 v128, v120, v121 op_sel:[0,0,1]
	v_cvt_pk_fp8_f32 v116, v112, v113 op_sel:[0,0,1]
	v_cvt_pk_fp8_f32 v100, v96, v97 op_sel:[0,0,1]
	v_cvt_pk_fp8_f32 v92, v88, v89 op_sel:[0,0,1]
	v_cvt_pk_fp8_f32 v84, v80, v81 op_sel:[0,0,1]
	v_add_co_u32_e32 v74, vcc, s27, v142
	v_cvt_pk_fp8_f32 v76, v72, v73 op_sel:[0,0,1]
	v_cvt_pk_fp8_f32 v77, v68, v69 op_sel:[0,0,1]
	v_addc_co_u32_e32 v75, vcc, 0, v143, vcc
	s_mov_b32 s27, 0x58000
	v_add_co_u32_e32 v66, vcc, s27, v142
	global_store_dwordx2 v[142:143], v[156:157], off
	s_nop 0
	v_addc_co_u32_e32 v67, vcc, 0, v143, vcc
	global_store_dwordx2 v[114:115], v[128:129], off
	global_store_dwordx2 v[106:107], v[116:117], off
	global_store_dwordx2 v[90:91], v[100:101], off
	global_store_dwordx2 v[82:83], v[92:93], off
	global_store_dwordx2 v[74:75], v[84:85], off
	global_store_dwordx2 v[66:67], v[76:77], off
	s_waitcnt lgkmcnt(0)
	v_mov_b32_e32 v66, v160
	v_mov_b32_e32 v67, v161
	v_mov_b32_e32 v68, v162
	v_mov_b32_e32 v69, v163
	v_mov_b32_e32 v70, v164
	v_mov_b32_e32 v71, v165
	v_mov_b32_e32 v72, v166
	v_mov_b32_e32 v73, v167
	v_mov_b32_e32 v77, v139
	v_mov_b32_e32 v76, v139
	v_lshl_add_u64 v[126:127], v[142:143], 0, s[40:41]
	s_mov_b64 s[40:41], 0x10000
	v_lshl_add_u64 v[114:115], v[142:143], 0, s[40:41]
	s_mov_b64 s[40:41], 0x18000
	v_lshl_add_u64 v[106:107], v[142:143], 0, s[40:41]
	s_mov_b64 s[40:41], 0x40000
	v_lshl_add_u64 v[98:99], v[142:143], 0, s[40:41]
	s_mov_b64 s[40:41], 0x48000
	v_lshl_add_u64 v[90:91], v[142:143], 0, s[40:41]
	s_mov_b64 s[40:41], 0x50000
	v_lshl_add_u64 v[82:83], v[142:143], 0, s[40:41]
	s_mov_b64 s[40:41], 0x58000
	v_lshl_add_u64 v[74:75], v[142:143], 0, s[40:41]
	s_mov_b64 s[40:41], -1
	s_and_b64 vcc, exec, s[2:3]
	v_pk_fma_f32 v[58:59], v[58:59], s[18:19], v[66:67] op_sel_hi:[1,0,1]
	s_nop 0
	v_pk_mul_f32 v[58:59], v[58:59], s[20:21] op_sel_hi:[1,0]
	v_pk_fma_f32 v[50:51], v[50:51], s[18:19], v[66:67] op_sel_hi:[1,0,1]
	v_cvt_pk_fp8_f32 v77, v58, v59
	v_pk_mul_f32 v[50:51], v[50:51], s[20:21] op_sel_hi:[1,0]
	v_mov_b32_e32 v59, v139
	v_pk_fma_f32 v[42:43], v[42:43], s[18:19], v[66:67] op_sel_hi:[1,0,1]
	v_cvt_pk_fp8_f32 v59, v50, v51
	v_pk_mul_f32 v[42:43], v[42:43], s[20:21] op_sel_hi:[1,0]
	v_mov_b32_e32 v51, v139
	v_pk_fma_f32 v[34:35], v[34:35], s[18:19], v[66:67] op_sel_hi:[1,0,1]
	v_cvt_pk_fp8_f32 v51, v42, v43
	v_pk_mul_f32 v[34:35], v[34:35], s[20:21] op_sel_hi:[1,0]
	v_mov_b32_e32 v43, v139
	v_pk_fma_f32 v[26:27], v[26:27], s[18:19], v[66:67] op_sel_hi:[1,0,1]
	v_cvt_pk_fp8_f32 v43, v34, v35
	v_pk_mul_f32 v[26:27], v[26:27], s[20:21] op_sel_hi:[1,0]
	v_mov_b32_e32 v35, v139
	v_pk_fma_f32 v[18:19], v[18:19], s[18:19], v[66:67] op_sel_hi:[1,0,1]
	v_cvt_pk_fp8_f32 v35, v26, v27
	v_pk_mul_f32 v[18:19], v[18:19], s[20:21] op_sel_hi:[1,0]
	v_mov_b32_e32 v27, v139
	v_pk_fma_f32 v[10:11], v[10:11], s[18:19], v[66:67] op_sel_hi:[1,0,1]
	v_pk_fma_f32 v[62:63], v[62:63], s[18:19], v[70:71] op_sel_hi:[1,0,1]
	v_pk_fma_f32 v[54:55], v[54:55], s[18:19], v[70:71] op_sel_hi:[1,0,1]
	v_pk_fma_f32 v[46:47], v[46:47], s[18:19], v[70:71] op_sel_hi:[1,0,1]
; __device__ __forceinline__ unsigned pk4_fp8(float a, float b, float c, float d) { int p = 0; p = __builtin_amdgcn_cvt_pk_fp8_f32(a, b, p, false); p = __builtin_amdgcn_cvt_pk_fp8_f32(c, d, p, true); return (unsigned)p; }
; #define PG8_BAR __builtin_amdgcn_s_barrier()
;     __device__ __forceinline__ void operator()(const f32x4 (&acc)[2][2][4][2], const Unit& u, int wr, int wc, int fr, int fq) const {
;         const int row0 = poff[u.e] + u.pm * BM + wr * 64 + fr, col0 = u.pn * BM + wc * 32 + 8 * fq;
;         const float* bp = bias + (size_t)u.e * D + col0;
; #pragma unroll
;         for (int bj = 0; bj < 2; ++bj) { const f32x4 b0 = *(const f32x4*)(bp + bj * HALF), b1 = *(const f32x4*)(bp + bj * HALF + 4);
; #pragma unroll
;             for (int ai = 0; ai < 2; ++ai)
; #pragma unroll
;                 for (int m = 0; m < 4; ++m) { unsigned char* rowp = YS + (size_t)(row0 + ai * HALF + m * 16) * D + col0 + bj * HALF;
;                     const f32x4 v0 = (acc[ai][bj][m][0] * WINV + b0) * YSCALE, v1 = (acc[ai][bj][m][1] * WINV + b1) * YSCALE;
;                     u32x2 w; w.x = pk4_fp8(v0[0], v0[1], v0[2], v0[3]); w.y = pk4_fp8(v1[0], v1[1], v1[2], v1[3]);
;                     *(u32x2*)rowp = w; } }
; template <class Epi, class Sched>
; __device__ __forceinline__ void gemm_phase(LAS unsigned char* lds, const Sched& S, const Epi& E) {
;     ...
;         if (!has_next) break;
; #pragma unroll
;         for (int a = 0; a < 2; ++a)
; #pragma unroll
;             for (int b = 0; b < 2; ++b)
; #pragma unroll
;                 for (int m = 0; m < 4; ++m)
; #pragma unroll
;                     for (int n = 0; n < 2; ++n) acc[a][b][m][n] = (f32x4){0.f, 0.f, 0.f, 0.f};
;         cur = nxt; cA = nA; cB = nB; ++ui;
;         if (wr == 1) PG8_BAR;
	v_pk_fma_f32 v[38:39], v[38:39], s[18:19], v[70:71] op_sel_hi:[1,0,1]
	v_pk_fma_f32 v[30:31], v[30:31], s[18:19], v[70:71] op_sel_hi:[1,0,1]
	v_pk_fma_f32 v[22:23], v[22:23], s[18:19], v[70:71] op_sel_hi:[1,0,1]
	v_cvt_pk_fp8_f32 v27, v18, v19
	v_pk_fma_f32 v[14:15], v[14:15], s[18:19], v[70:71] op_sel_hi:[1,0,1]
	v_pk_mul_f32 v[10:11], v[10:11], s[20:21] op_sel_hi:[1,0]
	v_mov_b32_e32 v19, v139
	v_pk_fma_f32 v[6:7], v[6:7], s[18:19], v[70:71] op_sel_hi:[1,0,1]
	v_pk_fma_f32 v[2:3], v[2:3], s[18:19], v[66:67] op_sel_hi:[1,0,1]
	v_pk_mul_f32 v[62:63], v[62:63], s[20:21] op_sel_hi:[1,0]
	v_pk_mul_f32 v[54:55], v[54:55], s[20:21] op_sel_hi:[1,0]
	v_mov_b32_e32 v58, v139
	v_pk_mul_f32 v[46:47], v[46:47], s[20:21] op_sel_hi:[1,0]
	v_mov_b32_e32 v50, v139
	v_pk_mul_f32 v[38:39], v[38:39], s[20:21] op_sel_hi:[1,0]
	v_mov_b32_e32 v42, v139
	v_pk_mul_f32 v[30:31], v[30:31], s[20:21] op_sel_hi:[1,0]
	v_mov_b32_e32 v34, v139
	v_pk_mul_f32 v[22:23], v[22:23], s[20:21] op_sel_hi:[1,0]
	v_mov_b32_e32 v26, v139
	v_pk_mul_f32 v[14:15], v[14:15], s[20:21] op_sel_hi:[1,0]
	v_mov_b32_e32 v18, v139
	v_cvt_pk_fp8_f32 v19, v10, v11
	v_pk_mul_f32 v[6:7], v[6:7], s[20:21] op_sel_hi:[1,0]
	v_pk_mul_f32 v[2:3], v[2:3], s[20:21] op_sel_hi:[1,0]
	v_mov_b32_e32 v10, v139
	v_mov_b32_e32 v11, v139
	v_cvt_pk_fp8_f32 v76, v62, v63
	v_cvt_pk_fp8_f32 v58, v54, v55
	v_cvt_pk_fp8_f32 v50, v46, v47
	v_cvt_pk_fp8_f32 v42, v38, v39
	v_cvt_pk_fp8_f32 v34, v30, v31
	v_cvt_pk_fp8_f32 v26, v22, v23
	v_cvt_pk_fp8_f32 v18, v14, v15
	v_cvt_pk_fp8_f32 v10, v6, v7
	v_cvt_pk_fp8_f32 v11, v2, v3
	v_pk_fma_f32 v[64:65], v[64:65], s[18:19], v[72:73] op_sel_hi:[1,0,1]
	v_pk_fma_f32 v[60:61], v[60:61], s[18:19], v[68:69] op_sel_hi:[1,0,1]
	v_pk_fma_f32 v[56:57], v[56:57], s[18:19], v[72:73] op_sel_hi:[1,0,1]
	v_pk_fma_f32 v[52:53], v[52:53], s[18:19], v[68:69] op_sel_hi:[1,0,1]
	v_pk_fma_f32 v[48:49], v[48:49], s[18:19], v[72:73] op_sel_hi:[1,0,1]
	v_pk_fma_f32 v[44:45], v[44:45], s[18:19], v[68:69] op_sel_hi:[1,0,1]
	v_pk_fma_f32 v[40:41], v[40:41], s[18:19], v[72:73] op_sel_hi:[1,0,1]
	v_pk_fma_f32 v[36:37], v[36:37], s[18:19], v[68:69] op_sel_hi:[1,0,1]
	v_pk_fma_f32 v[32:33], v[32:33], s[18:19], v[72:73] op_sel_hi:[1,0,1]
	v_pk_fma_f32 v[28:29], v[28:29], s[18:19], v[68:69] op_sel_hi:[1,0,1]
	v_pk_fma_f32 v[24:25], v[24:25], s[18:19], v[72:73] op_sel_hi:[1,0,1]
	v_pk_fma_f32 v[20:21], v[20:21], s[18:19], v[68:69] op_sel_hi:[1,0,1]
	v_pk_fma_f32 v[16:17], v[16:17], s[18:19], v[72:73] op_sel_hi:[1,0,1]
	v_pk_fma_f32 v[12:13], v[12:13], s[18:19], v[68:69] op_sel_hi:[1,0,1]
	v_pk_fma_f32 v[8:9], v[8:9], s[18:19], v[72:73] op_sel_hi:[1,0,1]
	v_pk_fma_f32 v[4:5], v[4:5], s[18:19], v[68:69] op_sel_hi:[1,0,1]
	v_pk_mul_f32 v[64:65], v[64:65], s[20:21] op_sel_hi:[1,0]
	v_pk_mul_f32 v[60:61], v[60:61], s[20:21] op_sel_hi:[1,0]
	v_pk_mul_f32 v[56:57], v[56:57], s[20:21] op_sel_hi:[1,0]
	v_pk_mul_f32 v[52:53], v[52:53], s[20:21] op_sel_hi:[1,0]
	v_pk_mul_f32 v[48:49], v[48:49], s[20:21] op_sel_hi:[1,0]
	v_pk_mul_f32 v[44:45], v[44:45], s[20:21] op_sel_hi:[1,0]
	v_pk_mul_f32 v[40:41], v[40:41], s[20:21] op_sel_hi:[1,0]
	v_pk_mul_f32 v[36:37], v[36:37], s[20:21] op_sel_hi:[1,0]
	v_pk_mul_f32 v[32:33], v[32:33], s[20:21] op_sel_hi:[1,0]
	v_pk_mul_f32 v[28:29], v[28:29], s[20:21] op_sel_hi:[1,0]
	v_pk_mul_f32 v[24:25], v[24:25], s[20:21] op_sel_hi:[1,0]
	v_pk_mul_f32 v[20:21], v[20:21], s[20:21] op_sel_hi:[1,0]
	v_pk_mul_f32 v[16:17], v[16:17], s[20:21] op_sel_hi:[1,0]
	v_pk_mul_f32 v[12:13], v[12:13], s[20:21] op_sel_hi:[1,0]
	v_pk_mul_f32 v[8:9], v[8:9], s[20:21] op_sel_hi:[1,0]
	v_pk_mul_f32 v[4:5], v[4:5], s[20:21] op_sel_hi:[1,0]
	v_cvt_pk_fp8_f32 v76, v64, v65 op_sel:[0,0,1]
	v_cvt_pk_fp8_f32 v77, v60, v61 op_sel:[0,0,1]
	v_cvt_pk_fp8_f32 v58, v56, v57 op_sel:[0,0,1]
	v_cvt_pk_fp8_f32 v59, v52, v53 op_sel:[0,0,1]
	v_cvt_pk_fp8_f32 v50, v48, v49 op_sel:[0,0,1]
	v_cvt_pk_fp8_f32 v51, v44, v45 op_sel:[0,0,1]
	v_cvt_pk_fp8_f32 v42, v40, v41 op_sel:[0,0,1]
	v_cvt_pk_fp8_f32 v43, v36, v37 op_sel:[0,0,1]
	v_cvt_pk_fp8_f32 v34, v32, v33 op_sel:[0,0,1]
	v_cvt_pk_fp8_f32 v35, v28, v29 op_sel:[0,0,1]
	v_cvt_pk_fp8_f32 v26, v24, v25 op_sel:[0,0,1]
	v_cvt_pk_fp8_f32 v27, v20, v21 op_sel:[0,0,1]
	v_cvt_pk_fp8_f32 v18, v16, v17 op_sel:[0,0,1]
	v_cvt_pk_fp8_f32 v19, v12, v13 op_sel:[0,0,1]
	v_cvt_pk_fp8_f32 v10, v8, v9 op_sel:[0,0,1]
	v_cvt_pk_fp8_f32 v11, v4, v5 op_sel:[0,0,1]
	global_store_dwordx2 v[142:143], v[76:77], off offset:128
	global_store_dwordx2 v[126:127], v[58:59], off offset:128
	global_store_dwordx2 v[114:115], v[50:51], off offset:128
	global_store_dwordx2 v[106:107], v[42:43], off offset:128
	global_store_dwordx2 v[98:99], v[34:35], off offset:128
	global_store_dwordx2 v[90:91], v[26:27], off offset:128
	global_store_dwordx2 v[82:83], v[18:19], off offset:128
	global_store_dwordx2 v[74:75], v[10:11], off offset:128
	s_cbranch_vccnz .LBB0_1455
	s_andn2_b64 vcc, exec, s[0:1]
	s_cbranch_vccnz .LBB0_1454
	s_barrier
	s_branch .LBB0_1454

; __global__ void __launch_bounds__(NT, 2) mk_fwd(Args args) {
	.amdhsa_kernel _Z6mk_fwd4Args
		.amdhsa_group_segment_fixed_size 0
		.amdhsa_private_segment_fixed_size 0
		.amdhsa_kernarg_size 424
		.amdhsa_user_sgpr_count 2
		.amdhsa_user_sgpr_dispatch_ptr 0
		.amdhsa_user_sgpr_queue_ptr 0
		.amdhsa_user_sgpr_kernarg_segment_ptr 1
		.amdhsa_user_sgpr_dispatch_id 0
		.amdhsa_user_sgpr_kernarg_preload_length 0
		.amdhsa_user_sgpr_kernarg_preload_offset 0
		.amdhsa_user_sgpr_private_segment_size 0
		.amdhsa_uses_dynamic_stack 0
		.amdhsa_enable_private_segment 0
		.amdhsa_system_sgpr_workgroup_id_x 1
		.amdhsa_system_sgpr_workgroup_id_y 0
		.amdhsa_system_sgpr_workgroup_id_z 0
		.amdhsa_system_sgpr_workgroup_info 0
		.amdhsa_system_vgpr_workitem_id 0
		.amdhsa_next_free_vgpr 256
		.amdhsa_next_free_sgpr 102
		.amdhsa_accum_offset 256
		.amdhsa_reserve_vcc 1
		.amdhsa_float_round_mode_32 0
		.amdhsa_float_round_mode_16_64 0
		.amdhsa_float_denorm_mode_32 3
		.amdhsa_float_denorm_mode_16_64 3
		.amdhsa_dx10_clamp 1
		.amdhsa_ieee_mode 1
		.amdhsa_fp16_overflow 0
		.amdhsa_tg_split 0
		.amdhsa_exception_fp_ieee_invalid_op 0
		.amdhsa_exception_fp_denorm_src 0
		.amdhsa_exception_fp_ieee_div_zero 0
		.amdhsa_exception_fp_ieee_overflow 0
		.amdhsa_exception_fp_ieee_underflow 0
		.amdhsa_exception_fp_ieee_inexact 0
		.amdhsa_exception_int_div_zero 0
	.end_amdhsa_kernel

; __global__ void __launch_bounds__(NT, 2) mk_fwd(Args args) {
amdhsa.kernels:
  - .agpr_count:     0
    .args:
      - .offset:         0
        .size:           168
        .value_kind:     by_value
      - .offset:         168
        .size:           4
        .value_kind:     hidden_block_count_x
      - .offset:         172
        .size:           4
        .value_kind:     hidden_block_count_y
      - .offset:         176
        .size:           4
        .value_kind:     hidden_block_count_z
      - .offset:         180
        .size:           2
        .value_kind:     hidden_group_size_x
      - .offset:         182
        .size:           2
        .value_kind:     hidden_group_size_y
      - .offset:         184
        .size:           2
        .value_kind:     hidden_group_size_z
      - .offset:         186
        .size:           2
        .value_kind:     hidden_remainder_x
      - .offset:         188
        .size:           2
        .value_kind:     hidden_remainder_y
      - .offset:         190
        .size:           2
        .value_kind:     hidden_remainder_z
      - .offset:         208
        .size:           8
        .value_kind:     hidden_global_offset_x
      - .offset:         216
        .size:           8
        .value_kind:     hidden_global_offset_y
      - .offset:         224
        .size:           8
        .value_kind:     hidden_global_offset_z
      - .offset:         232
        .size:           2
        .value_kind:     hidden_grid_dims
      - .offset:         288
        .size:           4
        .value_kind:     hidden_dynamic_lds_size
    .group_segment_fixed_size: 0
    .kernarg_segment_align: 8
    .kernarg_segment_size: 424
    .language:       OpenCL C
    .language_version:
      - 2
      - 0
    .max_flat_workgroup_size: 512
    .name:           _Z6mk_fwd4Args
    .private_segment_fixed_size: 0
    .sgpr_count:     108
    .sgpr_spill_count: 180
    .symbol:         _Z6mk_fwd4Args.kd
    .uniform_work_group_size: 1
    .uses_dynamic_stack: false
    .vgpr_count:     256
    .vgpr_spill_count: 0
    .wavefront_size: 64
